# baseline (speedup 1.0000x reference)
.Lno_anc:
	s_or_b64 exec, exec, s[8:9]
	v_mov_b32_e32 v7, 0x80
	s_waitcnt vmcnt(0)
	s_sub_u32 s26, 0x1ff, s2
	s_mul_i32 s26, s26, 7
	s_lshr_b32 s26, s26, 6
	s_min_u32 s26, s26, 64
	s_cmp_eq_u32 s26, 0
	s_cbranch_scc1 .Lhold_done
